# v14 plus batched router-bias dot products in late_prep and deferred scale/shift (PSH) fold in the router prologue
# speedup vs baseline: 1.0016x; 1.0016x over previous
; __device__ __forceinline__ void late_prep(const Args& a, unsigned char* lds_g, int gw, int NGW, int lane, int wave) {
;     ...
;         for (int q = gw; q < 4 * 48; q += NGW) { const int b = q / 48, j = q % 48; float sacc = 0.f;
;             if (j < 36) { for (int k = lane; k < 2048; k += 64) { const float wv = j < 32 ? a.in[I_WRE][(size_t)k * 32 + j] : a.in[I_WRG][(size_t)k * 4 + (j - 32)]; sacc += MODr[b * 12288 + 3 * 2048 + k] * wv; } }
;             sacc = wave_sum(sacc); if (lane == 0) RB[q] = sacc; }
.LBB0_204:
	s_mul_hi_i32 s0, s10, 0x2aaaaaab
	s_lshr_b32 s1, s0, 31
	s_ashr_i32 s0, s0, 3
	s_add_i32 s0, s0, s1
	s_mul_i32 s1, s0, 48
	s_sub_i32 s14, s10, s1
	s_cmp_gt_i32 s14, 35
	v_mov_b32_e32 v13, v1
	s_cbranch_scc1 .LBB0_208
	s_load_dwordx16 s[36:51], s[96:97], 0x80
	s_cmp_lt_i32 s14, 32
	s_cselect_b64 s[4:5], -1, 0
	s_movk_i32 s72, 0x400
	s_cselect_b32 s72, 0x2000, s72
	s_mov_b32 s73, 0
	s_lshl_b64 s[6:7], s[14:15], 2
	s_mulk_i32 s0, 0x3000
	s_waitcnt lgkmcnt(0)
	s_add_u32 s18, s46, s6
	s_addc_u32 s19, s47, s7
	s_ashr_i32 s7, s14, 31
	s_mov_b32 s6, s14
	s_lshl_b64 s[6:7], s[6:7], 2
	s_add_u32 s20, s48, s6
	s_addc_u32 s21, s49, s7
	v_mov_b32_e32 v13, 0
	s_mov_b64 s[22:23], 0
	v_mov_b32_e32 v2, v12
	v_mov_b32_e32 v14, v11
	v_mov_b32_e32 v0, v10
.LBB0_206:
	v_mov_b32_e32 v3, v1
	v_add_u32_e32 v15, s0, v14
	v_lshl_add_u64 v[18:19], v[2:3], 2, s[18:19]
	v_lshl_add_u64 v[16:17], v[0:1], 2, s[20:21]
	v_add_u32_e32 v20, 0x1840, v15
	v_lshl_add_u64 v[18:19], v[18:19], 0, s[16:17]
	v_ashrrev_i32_e32 v21, 31, v20
	v_cndmask_b32_e64 v17, v19, v17, s[4:5]
	v_cndmask_b32_e64 v16, v18, v16, s[4:5]
	v_lshl_add_u64 v[18:19], v[20:21], 2, s[12:13]
	global_load_dword v70, v[16:17], off
	v_lshl_add_u64 v[16:17], v[16:17], 0, s[72:73]
	global_load_dword v71, v[16:17], off
	v_lshl_add_u64 v[16:17], v[16:17], 0, s[72:73]
	global_load_dword v72, v[16:17], off
	v_lshl_add_u64 v[16:17], v[16:17], 0, s[72:73]
	global_load_dword v73, v[16:17], off
	v_lshl_add_u64 v[16:17], v[16:17], 0, s[72:73]
	global_load_dword v74, v[16:17], off
	v_lshl_add_u64 v[16:17], v[16:17], 0, s[72:73]
	global_load_dword v75, v[16:17], off
	v_lshl_add_u64 v[16:17], v[16:17], 0, s[72:73]
	global_load_dword v76, v[16:17], off
	v_lshl_add_u64 v[16:17], v[16:17], 0, s[72:73]
	global_load_dword v77, v[16:17], off
	global_load_dword v78, v[18:19], off
	global_load_dword v79, v[18:19], off offset:256
	global_load_dword v80, v[18:19], off offset:512
	global_load_dword v81, v[18:19], off offset:768
	global_load_dword v82, v[18:19], off offset:1024
	global_load_dword v83, v[18:19], off offset:1280
	global_load_dword v84, v[18:19], off offset:1536
	global_load_dword v85, v[18:19], off offset:1792
	v_add_u32_e32 v14, 0x200, v14
	v_cmp_lt_u32_e64 s[6:7], s25, v14
	v_add_u32_e32 v0, 0x4000, v0
	v_add_u32_e32 v2, 0x800, v2
	s_or_b64 s[22:23], s[6:7], s[22:23]
	s_waitcnt vmcnt(0)
	v_fmac_f32_e32 v13, v70, v78
	v_fmac_f32_e32 v13, v71, v79
	v_fmac_f32_e32 v13, v72, v80
	v_fmac_f32_e32 v13, v73, v81
	v_fmac_f32_e32 v13, v74, v82
	v_fmac_f32_e32 v13, v75, v83
	v_fmac_f32_e32 v13, v76, v84
	v_fmac_f32_e32 v13, v77, v85
	s_andn2_b64 exec, exec, s[22:23]
	s_cbranch_execnz .LBB0_206
	s_or_b64 exec, exec, s[22:23]

; __device__ __forceinline__ void phase_router(const Args& a, unsigned char* lds_g, int tid, int lane, int wave) {
;     ...
;     const bool shp = gridDim.x == 256; f32x4* PSH = (f32x4*)(lds_g + 65536);
;     if (shp) { const int t_ = wave * 64 + lane, c_ = 4 * t_, b_ = (32 * (int)blockIdx.x) >> 11;
;         const f32x4 gg = *(const f32x4*)(g + c_), sc = *(const f32x4*)(MOD + b_ * 12288 + 4 * 2048 + c_); PSH[t_] = gg * (sc + 1.f); PSH[512 + t_] = *(const f32x4*)(MOD + b_ * 12288 + 3 * 2048 + c_); }
.LBB0_969:
	s_load_dwordx8 s[88:95], s[96:97], 0xc0
	s_cmp_lt_i32 s86, 7
	s_cselect_b64 s[0:1], -1, 0
	s_and_b64 s[16:17], s[0:1], s[6:7]
	s_andn2_b64 vcc, exec, s[16:17]
	s_cbranch_vccnz .LBB0_1113
	s_add_u32 s2, s84, 0x100000
	s_addc_u32 s3, s85, 0
	s_cmpk_lg_i32 s82, 0x100
	v_readlane_b32 s0, v249, 1
	s_cselect_b64 s[18:19], -1, 0
	v_mbcnt_lo_u32_b32 v60, -1, 0
	v_mbcnt_hi_u32_b32 v60, -1, v60
	s_and_b64 vcc, exec, s[18:19]
	v_or_b32_e32 v0, s0, v60
	s_nop 0
	v_readfirstlane_b32 s4, v0
	s_cbranch_vccnz .LBB0_972
	s_lshr_b32 s0, s83, 6
	s_mulk_i32 s0, 0x3000
	s_ashr_i32 s1, s0, 31
	s_lshl_b64 s[0:1], s[0:1], 2
	s_add_u32 s0, s2, s0
	s_addc_u32 s1, s3, s1
	s_and_b32 s5, s4, 0xffffffc0
	s_waitcnt vmcnt(0)
	v_or_b32_e32 v12, s5, v60
	v_lshlrev_b32_e32 v0, 2, v12
	v_mov_b32_e32 v1, 0
	v_lshlrev_b64 v[4:5], 2, v[0:1]
	v_readlane_b32 s36, v249, 6
	v_readlane_b32 s44, v249, 14
	v_readlane_b32 s45, v249, 15
	v_lshl_add_u64 v[8:9], s[0:1], 0, v[4:5]
	s_mov_b32 s0, 0x8000
	v_lshl_add_u64 v[0:1], s[44:45], 0, v[4:5]
	v_add_co_u32_e32 v4, vcc, s0, v8
	global_load_dwordx4 v[222:225], v[0:1], off
	s_nop 0
	v_addc_co_u32_e32 v5, vcc, 0, v9, vcc
	global_load_dwordx4 v[226:229], v[4:5], off
	v_add_co_u32_e32 v8, vcc, 0x6000, v8
	v_lshl_add_u32 v234, v12, 4, 0
	s_nop 0
	v_addc_co_u32_e32 v9, vcc, 0, v9, vcc
	global_load_dwordx4 v[230:233], v[8:9], off
	v_add_u32_e32 v234, 0x10000, v234
	v_readlane_b32 s37, v249, 7
	v_readlane_b32 s38, v249, 8
	v_readlane_b32 s39, v249, 9
	v_readlane_b32 s40, v249, 10
	v_readlane_b32 s41, v249, 11
	v_readlane_b32 s42, v249, 12
	v_readlane_b32 s43, v249, 13
	v_readlane_b32 s46, v249, 16
	v_readlane_b32 s47, v249, 17
	v_readlane_b32 s48, v249, 18
	v_readlane_b32 s49, v249, 19
	v_readlane_b32 s50, v249, 20
	v_readlane_b32 s51, v249, 21

; __device__ __forceinline__ void phase_router(const Args& a, unsigned char* lds_g, int tid, int lane, int wave) {
;     ...
;     for (int tp = blockIdx.x; tp < NLAT / 32; tp += gridDim.x) {
;         const int tok0 = 32 * tp + 16 * slot, b = tok0 >> 11, kbase = wave * 256 + 8 * gq;
;         const bf16* xr0 = X1 + (size_t)(32 * tp + i) * D + kbase; const bf16* xr1 = xr0 + (size_t)16 * D;
;         const bf16* wh = WRh + ((size_t)(b * 48 + i) * 2048 + kbase); const bf16* wl = WRl + ((size_t)(b * 48 + i) * 2048 + kbase);
;         f32x4 ac[2][3]; float sq0 = 0.f, sq1 = 0.f;
; #pragma unroll
;         for (int s = 0; s < 2; ++s)
; #pragma unroll
;             for (int cb = 0; cb < 3; ++cb) ac[s][cb] = (f32x4){0.f, 0.f, 0.f, 0.f};
; #pragma unroll 4
;         for (int s8 = 0; s8 < 8; ++s8) {
.LBB0_975:
	s_lshl_b32 s31, s55, 5
	s_add_i32 s56, s31, s36
	s_ashr_i32 s30, s56, 11
	s_mul_i32 s4, s30, 48
	v_ashrrev_i32_e32 v107, 31, v106
	s_waitcnt vmcnt(3)
	v_or_b32_e32 v24, s4, v174
	v_lshlrev_b64 v[0:1], 12, v[106:107]
	v_ashrrev_i32_e32 v25, 31, v24
	v_lshl_add_u64 v[26:27], v[104:105], 0, v[0:1]
	v_lshlrev_b64 v[0:1], 12, v[24:25]
	s_mul_i32 s4, s30, 0x30000
	s_add_i32 s4, s4, s100
	v_lshl_add_u32 v0, v62, 2, s4
	v_mov_b32_e32 v1, 0
	v_lshl_add_u64 v[28:29], v[0:1], 0, s[84:85]
	s_mov_b64 s[4:5], 0
	v_mov_b32_e32 v0, 0
	v_mov_b32_e32 v1, v61
	v_mov_b32_e32 v2, v61
	v_mov_b32_e32 v3, v61
	v_mov_b32_e32 v4, 0
	v_mov_b32_e32 v5, v61
	v_mov_b32_e32 v6, v61
	v_mov_b32_e32 v7, v61
	v_mov_b32_e32 v8, 0
	v_mov_b32_e32 v9, v61
	v_mov_b32_e32 v10, v61
	v_mov_b32_e32 v11, v61
	v_mov_b32_e32 v12, 0
	v_mov_b32_e32 v13, v61
	v_mov_b32_e32 v14, v61
	v_mov_b32_e32 v15, v61
	v_mov_b32_e32 v16, 0
	v_mov_b32_e32 v17, v61
	v_mov_b32_e32 v18, v61
	v_mov_b32_e32 v19, v61
	v_mov_b32_e32 v20, 0
	v_mov_b32_e32 v21, v61
	v_mov_b32_e32 v22, v61
	v_mov_b32_e32 v23, v61
	v_mov_b32_e32 v30, 0
	v_mov_b32_e32 v31, v61
.LBB0_976:
	v_lshl_add_u64 v[34:35], v[26:27], 0, s[4:5]
	v_add_co_u32_e32 v162, vcc, s45, v34
	v_lshl_add_u64 v[32:33], s[4:5], 4, v[28:29]
	s_nop 0
	v_addc_co_u32_e32 v163, vcc, 0, v35, vcc
	v_add_co_u32_e32 v158, vcc, s46, v34
	s_add_u32 s4, s4, 0x100
	s_nop 0
	v_addc_co_u32_e32 v159, vcc, 0, v35, vcc
	v_add_co_u32_e32 v194, vcc, s47, v32
	s_addc_u32 s5, s5, 0
	s_nop 0
	v_addc_co_u32_e32 v195, vcc, 0, v33, vcc
	v_add_co_u32_e32 v198, vcc, s48, v32
	s_cmpk_eq_i32 s4, 0x200
	s_nop 0
	v_addc_co_u32_e32 v199, vcc, 0, v33, vcc
	v_add_co_u32_e32 v202, vcc, s49, v32
	s_nop 1
	v_addc_co_u32_e32 v203, vcc, 0, v33, vcc
	v_add_co_u32_e32 v206, vcc, s50, v32
	s_nop 1
	v_addc_co_u32_e32 v207, vcc, 0, v33, vcc
	v_add_co_u32_e32 v210, vcc, s51, v32
	s_nop 1
	v_addc_co_u32_e32 v211, vcc, 0, v33, vcc
	v_add_co_u32_e32 v214, vcc, s52, v32
	s_nop 1
	v_addc_co_u32_e32 v215, vcc, 0, v33, vcc
	global_load_dwordx4 v[32:35], v[162:163], off
	global_load_dwordx4 v[36:39], v[194:195], off
	global_load_dwordx4 v[40:43], v[158:159], off
	global_load_dwordx4 v[44:47], v[202:203], off
	global_load_dwordx4 v[48:51], v[198:199], off
	global_load_dwordx4 v[52:55], v[206:207], off
	global_load_dwordx4 v[56:59], v[214:215], off
	global_load_dwordx4 v[114:117], v[210:211], off
	global_load_dwordx4 v[118:121], v[162:163], off offset:64
	global_load_dwordx4 v[122:125], v[194:195], off offset:1024
	global_load_dwordx4 v[126:129], v[158:159], off offset:64
	global_load_dwordx4 v[130:133], v[202:203], off offset:1024
	global_load_dwordx4 v[134:137], v[198:199], off offset:1024
	global_load_dwordx4 v[138:141], v[206:207], off offset:1024
	global_load_dwordx4 v[142:145], v[214:215], off offset:1024
	global_load_dwordx4 v[146:149], v[210:211], off offset:1024
	global_load_dwordx4 v[150:153], v[158:159], off offset:128
	s_waitcnt vmcnt(15)
	v_mfma_f32_16x16x32_bf16 v[0:3], v[32:35], v[36:39], v[0:3]
	s_waitcnt vmcnt(14)
	v_and_b32_e32 v217, 0xffff0000, v42
	v_and_b32_e32 v216, 0xffff0000, v34
	v_lshlrev_b32_e32 v219, 16, v43
	s_waitcnt vmcnt(12)
	v_mfma_f32_16x16x32_bf16 v[16:19], v[40:43], v[48:51], v[16:19]
	v_mul_f32_e64 v216, v216, v216
	v_mul_f32_e64 v217, v217, v217
	v_lshlrev_b32_e32 v218, 16, v35
	s_waitcnt vmcnt(8)
	v_and_b32_e32 v220, 0xffff0000, v121
	v_mfma_f32_16x16x32_bf16 v[4:7], v[32:35], v[48:51], v[4:7]
	global_load_dwordx4 v[48:51], v[162:163], off offset:128
	s_waitcnt vmcnt(7)
	v_and_b32_e32 v221, 0xffff0000, v129
	v_mfma_f32_16x16x32_bf16 v[8:11], v[32:35], v[44:47], v[8:11]
	v_mfma_f32_16x16x32_bf16 v[12:15], v[40:43], v[36:39], v[12:15]
	global_load_dwordx4 v[36:39], v[194:195], off offset:2048
	v_mfma_f32_16x16x32_bf16 v[20:23], v[40:43], v[44:47], v[20:23]
	global_load_dwordx4 v[44:47], v[202:203], off offset:2048
	global_load_dwordx4 v[154:157], v[198:199], off offset:2048
	s_nop 0
	global_load_dwordx4 v[158:161], v[158:159], off offset:192
	s_nop 0
	global_load_dwordx4 v[162:165], v[162:163], off offset:192
	s_nop 0
	global_load_dwordx4 v[166:169], v[206:207], off offset:2048
	global_load_dwordx4 v[170:173], v[214:215], off offset:2048
	v_mfma_f32_16x16x32_bf16 v[16:19], v[40:43], v[114:117], v[16:19]
	global_load_dwordx4 v[194:197], v[194:195], off offset:3072
	s_nop 0
	global_load_dwordx4 v[198:201], v[198:199], off offset:3072
	s_nop 0
	global_load_dwordx4 v[202:205], v[202:203], off offset:3072
	v_mfma_f32_16x16x32_bf16 v[4:7], v[32:35], v[114:117], v[4:7]
	global_load_dwordx4 v[114:117], v[206:207], off offset:3072
	s_nop 0
	global_load_dwordx4 v[206:209], v[210:211], off offset:2048
	s_nop 0
	global_load_dwordx4 v[210:213], v[210:211], off offset:3072
	v_mfma_f32_16x16x32_bf16 v[0:3], v[32:35], v[52:55], v[0:3]
	v_mfma_f32_16x16x32_bf16 v[12:15], v[40:43], v[52:55], v[12:15]
	global_load_dwordx4 v[52:55], v[214:215], off offset:3072
	v_lshlrev_b32_e32 v215, 16, v40
	v_lshlrev_b32_e32 v214, 16, v32
	v_mfma_f32_16x16x32_bf16 v[8:11], v[32:35], v[56:59], v[8:11]
	v_mfma_f32_16x16x32_bf16 v[20:23], v[40:43], v[56:59], v[20:23]
	v_and_b32_e32 v57, 0xffff0000, v40
	v_and_b32_e32 v56, 0xffff0000, v32
	v_lshlrev_b32_e32 v59, 16, v41
	v_mfma_f32_16x16x32_bf16 v[0:3], v[118:121], v[122:125], v[0:3]
	v_and_b32_e32 v41, 0xffff0000, v41
	v_and_b32_e32 v40, 0xffff0000, v33
	v_pk_mul_f32 v[56:57], v[56:57], v[56:57]
	s_waitcnt vmcnt(20)
	v_mfma_f32_16x16x32_bf16 v[8:11], v[118:121], v[130:133], v[8:11]
	v_lshlrev_b32_e32 v58, 16, v33
	v_pk_mul_f32 v[40:41], v[40:41], v[40:41]
	v_pk_fma_f32 v[56:57], v[214:215], v[214:215], v[56:57]
	s_waitcnt vmcnt(19)
; __device__ __forceinline__ void phase_router(const Args& a, unsigned char* lds_g, int tid, int lane, int wave) {
;     ...
;         for (int s8 = 0; s8 < 8; ++s8) {
;             const v4u xb0 = *(const v4u*)(xr0 + 32 * s8), xb1 = *(const v4u*)(xr1 + 32 * s8);
;             const bf16x8_t h0 = *(const bf16x8_t*)(wh + 32 * s8), h1 = *(const bf16x8_t*)(wh + 16 * 2048 + 32 * s8), h2 = *(const bf16x8_t*)(wh + 32 * 2048 + 32 * s8);
;             const bf16x8_t l0 = *(const bf16x8_t*)(wl + 32 * s8), l1 = *(const bf16x8_t*)(wl + 16 * 2048 + 32 * s8), l2 = *(const bf16x8_t*)(wl + 32 * 2048 + 32 * s8);
;             const bf16x8_t xf0 = __builtin_bit_cast(bf16x8_t, xb0), xf1 = __builtin_bit_cast(bf16x8_t, xb1);
;             ac[0][0] = __builtin_amdgcn_mfma_f32_16x16x32_bf16(xf0, h0, ac[0][0], 0, 0, 0); ac[0][1] = __builtin_amdgcn_mfma_f32_16x16x32_bf16(xf0, h1, ac[0][1], 0, 0, 0); ac[0][2] = __builtin_amdgcn_mfma_f32_16x16x32_bf16(xf0, h2, ac[0][2], 0, 0, 0);
;             ac[1][0] = __builtin_amdgcn_mfma_f32_16x16x32_bf16(xf1, h0, ac[1][0], 0, 0, 0); ac[1][1] = __builtin_amdgcn_mfma_f32_16x16x32_bf16(xf1, h1, ac[1][1], 0, 0, 0); ac[1][2] = __builtin_amdgcn_mfma_f32_16x16x32_bf16(xf1, h2, ac[1][2], 0, 0, 0);
;             ac[0][0] = __builtin_amdgcn_mfma_f32_16x16x32_bf16(xf0, l0, ac[0][0], 0, 0, 0); ac[0][1] = __builtin_amdgcn_mfma_f32_16x16x32_bf16(xf0, l1, ac[0][1], 0, 0, 0); ac[0][2] = __builtin_amdgcn_mfma_f32_16x16x32_bf16(xf0, l2, ac[0][2], 0, 0, 0);
;             ac[1][0] = __builtin_amdgcn_mfma_f32_16x16x32_bf16(xf1, l0, ac[1][0], 0, 0, 0); ac[1][1] = __builtin_amdgcn_mfma_f32_16x16x32_bf16(xf1, l1, ac[1][1], 0, 0, 0); ac[1][2] = __builtin_amdgcn_mfma_f32_16x16x32_bf16(xf1, l2, ac[1][2], 0, 0, 0);
;             const unsigned xw0[4] = {xb0.x, xb0.y, xb0.z, xb0.w}, xw1[4] = {xb1.x, xb1.y, xb1.z, xb1.w};
; #pragma unroll
;             for (int e = 0; e < 4; ++e) { sq0 += bflo(xw0[e]) * bflo(xw0[e]) + bfhi(xw0[e]) * bfhi(xw0[e]); sq1 += bflo(xw1[e]) * bflo(xw1[e]) + bfhi(xw1[e]) * bfhi(xw1[e]); }
;         }
	v_mfma_f32_16x16x32_bf16 v[4:7], v[118:121], v[134:137], v[4:7]
	v_lshlrev_b32_e32 v33, 16, v42
	v_lshlrev_b32_e32 v32, 16, v34
	v_and_b32_e32 v43, 0xffff0000, v43
	v_mfma_f32_16x16x32_bf16 v[16:19], v[126:129], v[134:137], v[16:19]
	v_and_b32_e32 v42, 0xffff0000, v35
	v_pk_fma_f32 v[40:41], v[58:59], v[58:59], v[40:41]
	v_pk_add_f32 v[30:31], v[30:31], v[56:57]
	v_mfma_f32_16x16x32_bf16 v[12:15], v[126:129], v[122:125], v[12:15]
	v_and_b32_e32 v123, 0xffff0000, v126
	v_and_b32_e32 v122, 0xffff0000, v118
	v_pk_mul_f32 v[42:43], v[42:43], v[42:43]
	v_mfma_f32_16x16x32_bf16 v[20:23], v[126:129], v[130:133], v[20:23]
	v_fma_f32 v32, v32, v32, v216
	v_fma_f32 v33, v33, v33, v217
	v_pk_add_f32 v[30:31], v[40:41], v[30:31]
	v_lshlrev_b32_e32 v35, 16, v126
	s_waitcnt vmcnt(18)
	v_mfma_f32_16x16x32_bf16 v[0:3], v[118:121], v[138:141], v[0:3]
	v_lshlrev_b32_e32 v34, 16, v118
	v_and_b32_e32 v131, 0xffff0000, v127
	v_and_b32_e32 v130, 0xffff0000, v119
	s_waitcnt vmcnt(17)
	v_mfma_f32_16x16x32_bf16 v[8:11], v[118:121], v[142:145], v[8:11]
	v_lshlrev_b32_e32 v132, 16, v120
	v_and_b32_e32 v134, 0xffff0000, v120
	v_pk_fma_f32 v[42:43], v[218:219], v[218:219], v[42:43]
	s_waitcnt vmcnt(16)
	v_mfma_f32_16x16x32_bf16 v[4:7], v[118:121], v[146:149], v[4:7]
	v_add_f32_e64 v30, v32, v30
	v_add_f32_e64 v31, v33, v31
	v_lshlrev_b32_e32 v125, 16, v127
	v_lshlrev_b32_e32 v124, 16, v119
	v_mfma_f32_16x16x32_bf16 v[16:19], v[126:129], v[146:149], v[16:19]
	v_lshlrev_b32_e32 v133, 16, v128
	v_and_b32_e32 v135, 0xffff0000, v128
	v_pk_add_f32 v[30:31], v[42:43], v[30:31]
	v_mfma_f32_16x16x32_bf16 v[12:15], v[126:129], v[138:141], v[12:15]
	s_waitcnt vmcnt(14)
	v_lshlrev_b32_e32 v118, 16, v48
	v_and_b32_e32 v120, 0xffff0000, v48
	v_lshlrev_b32_e32 v138, 16, v49
	v_mfma_f32_16x16x32_bf16 v[20:23], v[126:129], v[142:145], v[20:23]
	v_and_b32_e32 v126, 0xffff0000, v49
	v_lshlrev_b32_e32 v128, 16, v50
	v_and_b32_e32 v140, 0xffff0000, v50
	s_waitcnt vmcnt(13)
	v_mfma_f32_16x16x32_bf16 v[0:3], v[48:51], v[36:39], v[0:3]
	v_lshlrev_b32_e32 v142, 16, v51
	v_and_b32_e32 v144, 0xffff0000, v51
	v_lshlrev_b32_e32 v137, 16, v129
	s_waitcnt vmcnt(12)
	v_mfma_f32_16x16x32_bf16 v[8:11], v[48:51], v[44:47], v[8:11]
	v_lshlrev_b32_e32 v136, 16, v121
	v_and_b32_e32 v121, 0xffff0000, v150
	v_lshlrev_b32_e32 v119, 16, v150
	s_waitcnt vmcnt(11)
	v_mfma_f32_16x16x32_bf16 v[4:7], v[48:51], v[154:157], v[4:7]
	v_and_b32_e32 v127, 0xffff0000, v151
	v_pk_mul_f32 v[120:121], v[120:121], v[120:121]
	v_lshlrev_b32_e32 v139, 16, v151
	v_mfma_f32_16x16x32_bf16 v[16:19], v[150:153], v[154:157], v[16:19]
	v_and_b32_e32 v141, 0xffff0000, v152
	v_pk_mul_f32 v[126:127], v[126:127], v[126:127]
	v_pk_fma_f32 v[118:119], v[118:119], v[118:119], v[120:121]
	v_mfma_f32_16x16x32_bf16 v[12:15], v[150:153], v[36:39], v[12:15]
	v_lshlrev_b32_e32 v129, 16, v152
	v_and_b32_e32 v145, 0xffff0000, v153
	v_pk_fma_f32 v[120:121], v[138:139], v[138:139], v[126:127]
	v_mfma_f32_16x16x32_bf16 v[20:23], v[150:153], v[44:47], v[20:23]
	v_lshlrev_b32_e32 v143, 16, v153
	s_waitcnt vmcnt(10)
	v_and_b32_e32 v149, 0xffff0000, v158
	s_waitcnt vmcnt(9)
	v_and_b32_e32 v148, 0xffff0000, v162
	s_waitcnt vmcnt(8)
	v_mfma_f32_16x16x32_bf16 v[0:3], v[48:51], v[166:169], v[0:3]
	v_lshlrev_b32_e32 v147, 16, v158
	v_lshlrev_b32_e32 v146, 16, v162
	v_and_b32_e32 v39, 0xffff0000, v159
	s_waitcnt vmcnt(7)
	v_mfma_f32_16x16x32_bf16 v[8:11], v[48:51], v[170:173], v[8:11]
	v_and_b32_e32 v38, 0xffff0000, v163
	v_lshlrev_b32_e32 v37, 16, v159
	v_lshlrev_b32_e32 v36, 16, v163
	s_waitcnt vmcnt(2)
	v_mfma_f32_16x16x32_bf16 v[4:7], v[48:51], v[206:209], v[4:7]
	v_mul_f32_e64 v48, v122, v122
	v_mul_f32_e64 v49, v123, v123
	v_pk_mul_f32 v[50:51], v[130:131], v[130:131]
	v_pk_fma_f32 v[34:35], v[34:35], v[34:35], v[48:49]
	v_mfma_f32_16x16x32_bf16 v[16:19], v[150:153], v[206:209], v[16:19]
	v_mul_f32_e64 v122, v134, v134
	v_mul_f32_e64 v123, v135, v135
	v_pk_fma_f32 v[48:49], v[124:125], v[124:125], v[50:51]
	v_pk_add_f32 v[30:31], v[30:31], v[34:35]
	v_mfma_f32_16x16x32_bf16 v[12:15], v[150:153], v[166:169], v[12:15]
	v_mul_f32_e64 v130, v220, v220
	v_mul_f32_e64 v131, v221, v221
	v_pk_fma_f32 v[50:51], v[132:133], v[132:133], v[122:123]
	v_pk_add_f32 v[30:31], v[48:49], v[30:31]
	v_mfma_f32_16x16x32_bf16 v[20:23], v[150:153], v[170:173], v[20:23]
	v_fma_f32 v58, v136, v136, v130
	v_fma_f32 v59, v137, v137, v131
	v_pk_add_f32 v[30:31], v[50:51], v[30:31]
	v_pk_mul_f32 v[134:135], v[140:141], v[140:141]
	v_pk_add_f32 v[30:31], v[58:59], v[30:31]
	v_mfma_f32_16x16x32_bf16 v[0:3], v[162:165], v[194:197], v[0:3]
	v_add_f32_e64 v30, v30, v118
	v_add_f32_e64 v31, v31, v119
	v_pk_mul_f32 v[140:141], v[144:145], v[144:145]
	v_pk_fma_f32 v[122:123], v[128:129], v[128:129], v[134:135]
	v_mfma_f32_16x16x32_bf16 v[8:11], v[162:165], v[202:205], v[8:11]
	v_add_f32_e64 v30, v120, v30
	v_add_f32_e64 v31, v121, v31
	v_pk_mul_f32 v[144:145], v[148:149], v[148:149]
	v_pk_fma_f32 v[124:125], v[142:143], v[142:143], v[140:141]
	v_mfma_f32_16x16x32_bf16 v[16:19], v[158:161], v[198:201], v[16:19]
	v_add_f32_e64 v30, v122, v30
	v_add_f32_e64 v31, v123, v31
	v_and_b32_e32 v47, 0xffff0000, v160
	v_and_b32_e32 v46, 0xffff0000, v164
	v_mfma_f32_16x16x32_bf16 v[4:7], v[162:165], v[198:201], v[4:7]
	v_mul_f32_e64 v38, v38, v38
	v_mul_f32_e64 v39, v39, v39
	v_pk_fma_f32 v[126:127], v[146:147], v[146:147], v[144:145]
	v_pk_add_f32 v[30:31], v[124:125], v[30:31]
	v_mfma_f32_16x16x32_bf16 v[12:15], v[158:161], v[194:197], v[12:15]
	v_lshlrev_b32_e32 v45, 16, v160
	v_lshlrev_b32_e32 v44, 16, v164
	v_and_b32_e32 v157, 0xffff0000, v161
	v_mfma_f32_16x16x32_bf16 v[20:23], v[158:161], v[202:205], v[20:23]
	v_and_b32_e32 v156, 0xffff0000, v165
	v_pk_mul_f32 v[46:47], v[46:47], v[46:47]
	v_pk_fma_f32 v[36:37], v[36:37], v[36:37], v[38:39]
	v_mfma_f32_16x16x32_bf16 v[0:3], v[162:165], v[114:117], v[0:3]
	v_add_f32_e64 v30, v30, v126
	v_add_f32_e64 v31, v31, v127
	v_lshlrev_b32_e32 v155, 16, v161
	v_lshlrev_b32_e32 v154, 16, v165
	s_waitcnt vmcnt(0)
	v_mfma_f32_16x16x32_bf16 v[8:11], v[162:165], v[52:55], v[8:11]
	v_mul_f32_e64 v148, v156, v156
	v_mul_f32_e64 v149, v157, v157
	v_pk_fma_f32 v[38:39], v[44:45], v[44:45], v[46:47]
	v_pk_add_f32 v[30:31], v[36:37], v[30:31]
	v_mfma_f32_16x16x32_bf16 v[16:19], v[158:161], v[210:213], v[16:19]
	v_fma_f32 v44, v154, v154, v148
	v_fma_f32 v45, v155, v155, v149
	v_pk_add_f32 v[30:31], v[38:39], v[30:31]
	v_mfma_f32_16x16x32_bf16 v[4:7], v[162:165], v[210:213], v[4:7]
	v_add_f32_e64 v30, v44, v30
	v_add_f32_e64 v31, v45, v31
	v_mfma_f32_16x16x32_bf16 v[12:15], v[158:161], v[114:117], v[12:15]
	v_mfma_f32_16x16x32_bf16 v[20:23], v[158:161], v[52:55], v[20:23]
	s_cbranch_scc0 .LBB0_976
; __device__ __forceinline__ void phase_router(const Args& a, unsigned char* lds_g, int tid, int lane, int wave) {
;     ...
;     if (shp) { const int t_ = wave * 64 + lane, c_ = 4 * t_, b_ = (32 * (int)blockIdx.x) >> 11;
;         const f32x4 gg = *(const f32x4*)(g + c_), sc = *(const f32x4*)(MOD + b_ * 12288 + 4 * 2048 + c_); PSH[t_] = gg * (sc + 1.f); PSH[512 + t_] = *(const f32x4*)(MOD + b_ * 12288 + 3 * 2048 + c_); }
;     ...
;         sq0 += __shfl_xor(sq0, 16); sq0 += __shfl_xor(sq0, 32); sq1 += __shfl_xor(sq1, 16); sq1 += __shfl_xor(sq1, 32);
; #pragma unroll
;         for (int s = 0; s < 2; ++s)
; #pragma unroll
;             for (int cb = 0; cb < 3; ++cb) PART[((s * 8 + wave) * 3 + cb) * 64 + lane] = ac[s][cb];
;         if (gq == 0) { SSQP[(0 * 8 + wave) * 16 + i] = sq0; SSQP[(1 * 8 + wave) * 16 + i] = sq1; }
	s_and_b64 vcc, exec, s[18:19]
	s_cbranch_vccnz .Lpsh_skip
	s_waitcnt vmcnt(0)
	v_pk_add_f32 v[228:229], v[228:229], 1.0 op_sel_hi:[1,0]
	v_pk_add_f32 v[226:227], v[226:227], 1.0 op_sel_hi:[1,0]
	v_pk_mul_f32 v[224:225], v[224:225], v[228:229]
	v_pk_mul_f32 v[222:223], v[222:223], v[226:227]
	ds_write_b128 v234, v[222:225]
	ds_write_b128 v234, v[230:233] offset:8192
.Lpsh_skip:
	ds_bpermute_b32 v26, v175, v30
	ds_bpermute_b32 v27, v175, v31
	v_add_u32_e32 v32, s38, v64
	ds_write_b128 v32, v[0:3]
	ds_write_b128 v32, v[4:7] offset:1024
	ds_write_b128 v32, v[8:11] offset:2048
	ds_write_b128 v32, v[12:15] offset:24576
	ds_write_b128 v32, v[16:19] offset:25600
	ds_write_b128 v32, v[20:23] offset:26624
	s_waitcnt lgkmcnt(0)
	v_add_f32_e32 v26, v30, v26
	v_add_f32_e32 v27, v31, v27
	ds_bpermute_b32 v28, v176, v26
	ds_bpermute_b32 v29, v176, v27
	s_and_saveexec_b64 s[4:5], s[0:1]
	s_cbranch_execz .LBB0_979
	s_waitcnt lgkmcnt(1)
	v_add_f32_e32 v0, v26, v28
	s_waitcnt lgkmcnt(0)
	v_add_f32_e32 v1, v27, v29
	ds_write_b32 v65, v0 offset:49152
	ds_write_b32 v177, v1 offset:49664
